# P + one static s_setprio 1 for waves 0-3 (the first-dispatched half) for the whole attention phase, reset at the phase exit
# speedup vs baseline: 1.0023x; 1.0023x over previous
.LBB0_1590:
	s_cmp_gt_i32 s34, 17
	s_cselect_b64 s[2:3], -1, 0
	s_cmp_lt_i32 s35, 18
	s_cselect_b64 s[4:5], -1, 0
	s_or_b64 s[2:3], s[2:3], s[4:5]
	s_and_b64 vcc, exec, s[2:3]
	s_cbranch_vccnz .LBB0_1700
	s_cmp_ge_u32 s11, 4
	s_cbranch_scc1 .Lattp_1
	s_setprio 1
.Lattp_1:
	s_load_dword s48, s[0:1], 0xd0
	s_add_u32 s8, s0, 0xd0
	s_addc_u32 s9, s1, 0
	s_and_b32 s49, s33, 0xffffffc0
	s_mov_b32 s12, 0
	s_movk_i32 s50, 0xc0
	s_mov_b32 s30, 0x300000
	v_mov_b32_e32 v185, 0
	s_mov_b32 s51, 0x2aaaaaab
	s_movk_i32 s52, 0x2000
	s_movk_i32 s53, 0x50
	s_mov_b32 s31, 0x20000
	s_mov_b32 s38, 0x200000
	s_movk_i32 s54, 0x3000
	s_movk_i32 s55, 0x6000
	s_movk_i32 s56, 0xd0
	s_mov_b32 s57, 0x9000
	v_mov_b32_e32 v190, 0x7c7c7c7c
	v_mov_b32_e32 v191, 0x7f7f7f7f
	s_mov_b32 s58, 0x43e00000
	s_movk_i32 s59, 0x7fff
	s_mov_b64 s[40:41], 0x2d000000
	s_mov_b32 s60, 0
	s_branch .LBB0_1594

.LBB0_1700:
	s_setprio 0
	s_cmp_gt_i32 s34, 18
	s_cselect_b64 s[2:3], -1, 0
	s_cmp_lt_i32 s35, 19
	s_cselect_b64 s[4:5], -1, 0
	s_or_b64 s[2:3], s[2:3], s[4:5]
	s_and_b64 vcc, exec, s[2:3]
	s_cbranch_vccnz .LBB0_1809
	s_mov_b32 s2, 24
	s_lshl_b32 s2, s2, 3
	s_add_i32 s2, s2, 0
	s_add_i32 s2, s2, 0x201c0
	v_mov_b32_e32 v0, s2
	s_waitcnt vmcnt(0) lgkmcnt(0)
	ds_read_b32 v1, v0
	ds_read_b32 v0, v0 offset:4
	s_load_dword s42, s[0:1], 0xd0
	s_mov_b32 s49, s10
	s_waitcnt lgkmcnt(0)
	v_readfirstlane_b32 s16, v1
	v_readfirstlane_b32 s17, v0
	s_add_u32 s45, s16, 0x2d000000
	s_addc_u32 s46, s17, 0
	s_add_u32 s47, s16, 0x1a00000
	s_addc_u32 s48, s17, 0
	s_add_u32 s6, s0, 0xd0
	s_mov_b32 s44, s42
	s_addc_u32 s7, s1, 0
	s_and_b32 s43, s33, 0xffffffc0
	v_mbcnt_lo_u32_b32 v8, -1, 0
	v_mbcnt_hi_u32_b32 v8, -1, v8
	v_mbcnt_lo_u32_b32 v9, -1, 0
	v_mbcnt_hi_u32_b32 v9, -1, v9
	s_cmpk_lt_i32 s49, 0x200
	v_add_u32_e32 v0, s43, v9
	s_cselect_b64 s[2:3], -1, 0
	s_cmpk_gt_i32 s49, 0x1ff
	v_readfirstlane_b32 s20, v0
	s_cbranch_scc1 .LBB0_1704
	s_ashr_i32 s4, s49, 31
	s_lshr_b32 s4, s4, 29
	s_add_i32 s12, s49, s4
	s_and_b32 s4, s12, -8
	s_sub_i32 s8, s49, s4
	s_cmp_gt_i32 s8, -1
	s_cbranch_scc0 .LBB0_1705
	s_lshl_b32 s9, s8, 6
	s_ashr_i32 s4, s12, 3
	s_cbranch_execz .LBB0_1706
	s_branch .LBB0_1707

.LBB0_3864:
	s_cmp_gt_i32 s34, 41
	s_cselect_b64 s[2:3], -1, 0
	s_cmp_lt_i32 s35, 42
	s_cselect_b64 s[4:5], -1, 0
	s_or_b64 s[2:3], s[2:3], s[4:5]
	s_and_b64 vcc, exec, s[2:3]
	s_cbranch_vccnz .LBB0_3974
	s_cmp_ge_u32 s11, 4
	s_cbranch_scc1 .Lattp_0
	s_setprio 1

.LBB0_3974:
	s_setprio 0
	s_cmp_gt_i32 s34, 42
	s_cselect_b64 s[2:3], -1, 0
	s_cmp_lt_i32 s35, 43
	s_cselect_b64 s[4:5], -1, 0
	s_or_b64 s[2:3], s[2:3], s[4:5]
	s_and_b64 vcc, exec, s[2:3]
	s_cbranch_vccnz .LBB0_4083
	s_mov_b32 s2, 24
	s_lshl_b32 s2, s2, 3
	s_add_i32 s2, s2, 0
	s_add_i32 s2, s2, 0x201c0
	v_mov_b32_e32 v0, s2
	s_waitcnt vmcnt(0) lgkmcnt(0)
	ds_read_b32 v1, v0
	ds_read_b32 v0, v0 offset:4
	s_load_dword s42, s[0:1], 0xd0
	s_mov_b32 s49, s10
	s_waitcnt lgkmcnt(0)
	v_readfirstlane_b32 s16, v1
	v_readfirstlane_b32 s17, v0
	s_add_u32 s45, s16, 0x2d000000
	s_addc_u32 s46, s17, 0
	s_add_u32 s47, s16, 0x1c00000
	s_addc_u32 s48, s17, 0
	s_add_u32 s6, s0, 0xd0
	s_mov_b32 s44, s42
	s_addc_u32 s7, s1, 0
	s_and_b32 s43, s33, 0xffffffc0
	v_mbcnt_lo_u32_b32 v8, -1, 0
	v_mbcnt_hi_u32_b32 v8, -1, v8
	v_mbcnt_lo_u32_b32 v9, -1, 0
	v_mbcnt_hi_u32_b32 v9, -1, v9
	s_cmpk_lt_i32 s49, 0x200
	v_add_u32_e32 v0, s43, v9
	s_cselect_b64 s[2:3], -1, 0
	s_cmpk_gt_i32 s49, 0x1ff
	v_readfirstlane_b32 s20, v0
	s_cbranch_scc1 .LBB0_3978
	s_ashr_i32 s4, s49, 31
	s_lshr_b32 s4, s4, 29
	s_add_i32 s12, s49, s4
	s_and_b32 s4, s12, -8
	s_sub_i32 s8, s49, s4
	s_cmp_gt_i32 s8, -1
	s_cbranch_scc0 .LBB0_3979
	s_lshl_b32 s9, s8, 6
	s_ashr_i32 s4, s12, 3
	s_cbranch_execz .LBB0_3980
	s_branch .LBB0_3981
